# speedup vs baseline: 1.0146x; 1.0146x over previous
.LBB0_78:
	s_or_b64 exec, exec, s[0:1]
	v_readfirstlane_b32 s0, v63
	s_lshl_b32 s1, s0, 2
	s_and_b32 s1, s1, 60
	s_ashr_i32 s24, s0, 4
	s_add_i32 s24, s24, s1
	s_add_i32 s24, s24, 1
	s_cmp_lt_i32 s0, 48
	s_cselect_b32 s25, s24, -1
	s_mov_b32 s26, s36
	s_mov_b32 s27, s35
	s_cmp_lt_i32 s25, 0
	s_cbranch_scc1 .Lnl_nopf
	s_lshl_b32 s0, s25, 5
	s_add_i32 s1, s0, 0x14400
	v_mov_b32_e32 v64, s1
	ds_read_b128 v[118:121], v64
	ds_read_b32 v122, v64 offset:16
	v_add_u32_e32 v65, s0, v111
	ds_read2_b32 v[124:125], v65 offset1:4
	s_lshl_b32 s0, s25, 8
	v_add_u32_e32 v63, s0, v113
	ds_read_b128 v[86:89], v63
	ds_read_b128 v[90:93], v63 offset:16
	ds_read_b128 v[94:97], v63 offset:32
	ds_read_b128 v[98:101], v63 offset:48
.Lnl_nopf:
	s_waitcnt vmcnt(0) lgkmcnt(0)
	v_pk_add_f32 v[102:103], v[6:7], v[10:11]
	v_pk_add_f32 v[104:105], v[8:9], v[12:13]
	s_cmp_lt_i32 s25, 0
	s_cbranch_scc1 .Lnl_nocat
	v_readfirstlane_b32 s27, v118
	v_readfirstlane_b32 s26, v119
	v_mov_b64_e32 v[6:7], 0
	v_mov_b64_e32 v[8:9], 0
	v_mov_b64_e32 v[10:11], 0
	v_mov_b64_e32 v[12:13], 0
	v_cmp_gt_i32_e32 vcc, s26, v106
	s_and_saveexec_b64 s[0:1], vcc
	s_cbranch_execz .Lnl_c0
	v_lshl_or_b32 v63, v124, 8, v107
	global_load_dwordx4 v[6:9], v63, s[18:19] sc1
.Lnl_c0:
	s_or_b64 exec, exec, s[0:1]
	v_cmp_gt_i32_e32 vcc, s26, v112
	s_and_saveexec_b64 s[0:1], vcc
	s_cbranch_execz .Lnl_c1
	v_lshl_or_b32 v63, v125, 8, v107
	global_load_dwordx4 v[10:13], v63, s[18:19] sc1
.Lnl_c1:
	s_or_b64 exec, exec, s[0:1]
	v_cndmask_b32_e64 v64, v122, v121, s[12:13]
	v_cndmask_b32_e64 v64, v64, v120, s[14:15]
	v_lshl_or_b32 v64, v64, 8, v107
	v_mov_b32_e32 v65, v62
	v_lshl_add_u64 v[64:65], v[0:1], 0, v[64:65]
.Lnl_nocat:
	ds_bpermute_b32 v118, v108, v2
	ds_bpermute_b32 v115, v108, v3
	ds_bpermute_b32 v114, v108, v4
	ds_bpermute_b32 v127, v108, v5
	ds_bpermute_b32 v124, v109, v2
	ds_bpermute_b32 v126, v109, v3
	ds_bpermute_b32 v125, v109, v4
	ds_bpermute_b32 v123, v109, v5
	ds_bpermute_b32 v120, v110, v2
	ds_bpermute_b32 v122, v110, v3
	ds_bpermute_b32 v121, v110, v4
	ds_bpermute_b32 v119, v110, v5
	s_cmp_lt_i32 s25, 0
	s_cbranch_scc1 .Lnl_nomisc
	v_mov_b64_e32 v[2:3], 0
	v_mov_b64_e32 v[4:5], 0
	s_and_saveexec_b64 s[0:1], s[16:17]
	global_load_dwordx4 v[2:5], v[64:65], off sc0 nt
	s_or_b64 exec, exec, s[0:1]
.Lnl_nomisc:
	s_add_i32 s1, s35, 3
	s_lshr_b32 s1, s1, 2
	v_mov_b64_e32 v[82:83], v[14:15]
	v_mov_b64_e32 v[84:85], v[16:17]
	s_cmp_lt_u32 s1, 2
	s_cbranch_scc1 .Lnl_red_done
	v_pk_add_f32 v[82:83], v[82:83], v[18:19]
	v_pk_add_f32 v[84:85], v[84:85], v[20:21]
	s_cmp_lt_u32 s1, 3
	s_cbranch_scc1 .Lnl_red_done
	v_pk_add_f32 v[82:83], v[82:83], v[22:23]
	v_pk_add_f32 v[84:85], v[84:85], v[24:25]
	s_cmp_lt_u32 s1, 4
	s_cbranch_scc1 .Lnl_red_done
	v_pk_add_f32 v[82:83], v[82:83], v[26:27]
	v_pk_add_f32 v[84:85], v[84:85], v[28:29]
	s_cmp_lt_u32 s1, 5
	s_cbranch_scc1 .Lnl_red_done
	v_pk_add_f32 v[82:83], v[82:83], v[30:31]
	v_pk_add_f32 v[84:85], v[84:85], v[32:33]
	s_cmp_lt_u32 s1, 6
	s_cbranch_scc1 .Lnl_red_done
	v_pk_add_f32 v[82:83], v[82:83], v[34:35]
	v_pk_add_f32 v[84:85], v[84:85], v[36:37]
	s_cmp_lt_u32 s1, 7
	s_cbranch_scc1 .Lnl_red_done
	v_pk_add_f32 v[82:83], v[82:83], v[38:39]
	v_pk_add_f32 v[84:85], v[84:85], v[40:41]
	s_cmp_lt_u32 s1, 8
	s_cbranch_scc1 .Lnl_red_done
	v_pk_add_f32 v[82:83], v[82:83], v[42:43]
	v_pk_add_f32 v[84:85], v[84:85], v[44:45]
	s_cmp_lt_u32 s1, 9
	s_cbranch_scc1 .Lnl_red_done
	v_pk_add_f32 v[82:83], v[82:83], v[46:47]
	v_pk_add_f32 v[84:85], v[84:85], v[48:49]
	s_cmp_lt_u32 s1, 10
	s_cbranch_scc1 .Lnl_red_done
	v_pk_add_f32 v[82:83], v[82:83], v[50:51]
	v_pk_add_f32 v[84:85], v[84:85], v[52:53]
	s_cmp_lt_u32 s1, 11
	s_cbranch_scc1 .Lnl_red_done
	v_pk_add_f32 v[82:83], v[82:83], v[54:55]
	v_pk_add_f32 v[84:85], v[84:85], v[56:57]
	s_cmp_lt_u32 s1, 12
	s_cbranch_scc1 .Lnl_red_done
	v_pk_add_f32 v[82:83], v[82:83], v[58:59]
	v_pk_add_f32 v[84:85], v[84:85], v[60:61]
	s_cmp_lt_u32 s1, 13
	s_cbranch_scc1 .Lnl_red_done
	v_pk_add_f32 v[82:83], v[82:83], v[66:67]
	v_pk_add_f32 v[84:85], v[84:85], v[68:69]
	s_cmp_lt_u32 s1, 14
	s_cbranch_scc1 .Lnl_red_done
	v_pk_add_f32 v[82:83], v[82:83], v[70:71]
	v_pk_add_f32 v[84:85], v[84:85], v[72:73]
	s_cmp_lt_u32 s1, 15
	s_cbranch_scc1 .Lnl_red_done
	v_pk_add_f32 v[82:83], v[82:83], v[74:75]
	v_pk_add_f32 v[84:85], v[84:85], v[76:77]
	s_cmp_lt_u32 s1, 16
	s_cbranch_scc1 .Lnl_red_done
	v_pk_add_f32 v[82:83], v[82:83], v[78:79]
	v_pk_add_f32 v[84:85], v[84:85], v[80:81]
.Lnl_red_done:
	s_cmp_lt_i32 s25, 0
	s_cbranch_scc1 .Lnl_t_done
	s_lshr_b32 s38, s27, 2
	s_and_b32 s39, s27, 3
	s_lshl_b32 s39, s39, 4
	s_cmp_gt_u32 s38, 0
	s_cbranch_scc0 .Lnl_tp0
	v_lshl_or_b32 v63, v86, 8, v107
	global_load_dwordx4 v[14:17], v63, s[28:29] sc0 nt
	s_cmp_gt_u32 s38, 1
	s_cbranch_scc0 .Lnl_tp1
	v_lshl_or_b32 v63, v87, 8, v107
	global_load_dwordx4 v[18:21], v63, s[28:29] sc0 nt
	s_cmp_gt_u32 s38, 2
	s_cbranch_scc0 .Lnl_tp2
	v_lshl_or_b32 v63, v88, 8, v107
	global_load_dwordx4 v[22:25], v63, s[28:29] sc0 nt
	s_cmp_gt_u32 s38, 3
	s_cbranch_scc0 .Lnl_tp3
	v_lshl_or_b32 v63, v89, 8, v107
	global_load_dwordx4 v[26:29], v63, s[28:29] sc0 nt
	s_cmp_gt_u32 s38, 4
	s_cbranch_scc0 .Lnl_tp4
	v_lshl_or_b32 v63, v90, 8, v107
	global_load_dwordx4 v[30:33], v63, s[28:29] sc0 nt
	s_cmp_gt_u32 s38, 5
	s_cbranch_scc0 .Lnl_tp5
	v_lshl_or_b32 v63, v91, 8, v107
	global_load_dwordx4 v[34:37], v63, s[28:29] sc0 nt
	s_cmp_gt_u32 s38, 6
	s_cbranch_scc0 .Lnl_tp6
	v_lshl_or_b32 v63, v92, 8, v107
	global_load_dwordx4 v[38:41], v63, s[28:29] sc0 nt
	s_cmp_gt_u32 s38, 7
	s_cbranch_scc0 .Lnl_tp7
	v_lshl_or_b32 v63, v93, 8, v107
	global_load_dwordx4 v[42:45], v63, s[28:29] sc0 nt
	s_cmp_gt_u32 s38, 8
	s_cbranch_scc0 .Lnl_tp8
	v_lshl_or_b32 v63, v94, 8, v107
	global_load_dwordx4 v[46:49], v63, s[28:29] sc0 nt
	s_cmp_gt_u32 s38, 9
	s_cbranch_scc0 .Lnl_tp9
	v_lshl_or_b32 v63, v95, 8, v107
	global_load_dwordx4 v[50:53], v63, s[28:29] sc0 nt
	s_cmp_gt_u32 s38, 10
	s_cbranch_scc0 .Lnl_tp10
	v_lshl_or_b32 v63, v96, 8, v107
	global_load_dwordx4 v[54:57], v63, s[28:29] sc0 nt
	s_cmp_gt_u32 s38, 11
	s_cbranch_scc0 .Lnl_tp11
	v_lshl_or_b32 v63, v97, 8, v107
	global_load_dwordx4 v[58:61], v63, s[28:29] sc0 nt
	s_cmp_gt_u32 s38, 12
	s_cbranch_scc0 .Lnl_tp12
	v_lshl_or_b32 v63, v98, 8, v107
	global_load_dwordx4 v[66:69], v63, s[28:29] sc0 nt
	s_cmp_gt_u32 s38, 13
	s_cbranch_scc0 .Lnl_tp13
	v_lshl_or_b32 v63, v99, 8, v107
	global_load_dwordx4 v[70:73], v63, s[28:29] sc0 nt
	s_cmp_gt_u32 s38, 14
	s_cbranch_scc0 .Lnl_tp14
	v_lshl_or_b32 v63, v100, 8, v107
	global_load_dwordx4 v[74:77], v63, s[28:29] sc0 nt
	s_cmp_gt_u32 s38, 15
	s_cbranch_scc0 .Lnl_tp15
	v_lshl_or_b32 v63, v101, 8, v107
	global_load_dwordx4 v[78:81], v63, s[28:29] sc0 nt
.Lnl_t_done:
	v_mov_b32_e32 v63, v102
	s_nop 1
	v_permlane16_swap_b32_e32 v102, v63
	v_add_f32_e32 v90, v102, v63
	v_mov_b32_e32 v63, v103
	s_nop 1
	v_permlane16_swap_b32_e32 v103, v63
	v_add_f32_e32 v91, v103, v63
	v_mov_b32_e32 v63, v104
	s_nop 1
	v_permlane16_swap_b32_e32 v104, v63
	v_add_f32_e32 v94, v104, v63
	v_mov_b32_e32 v63, v105
	s_nop 1
	v_permlane16_swap_b32_e32 v105, v63
	v_add_f32_e32 v95, v105, v63
	v_mov_b32_e32 v63, v82
	s_nop 1
	v_permlane16_swap_b32_e32 v82, v63
	v_add_f32_e32 v98, v82, v63
	v_mov_b32_e32 v63, v83
	s_nop 1
	v_permlane16_swap_b32_e32 v83, v63
	v_add_f32_e32 v99, v83, v63
	v_mov_b32_e32 v63, v84
	s_nop 1
	v_permlane16_swap_b32_e32 v84, v63
	v_add_f32_e32 v102, v84, v63
	v_mov_b32_e32 v63, v85
	s_nop 1
	v_permlane16_swap_b32_e32 v85, v63
	v_add_f32_e32 v103, v85, v63
	v_mov_b32_e32 v92, v90
	v_mov_b32_e32 v93, v91
	v_mov_b32_e32 v96, v94
	v_mov_b32_e32 v97, v95
	v_mov_b32_e32 v100, v98
	v_mov_b32_e32 v101, v99
	v_mov_b32_e32 v104, v102
	v_mov_b32_e32 v105, v103
	s_nop 1
	v_permlane32_swap_b32_e32 v90, v92
	v_permlane32_swap_b32_e32 v91, v93
	v_permlane32_swap_b32_e32 v94, v96
	v_permlane32_swap_b32_e32 v95, v97
	v_permlane32_swap_b32_e32 v98, v100
	v_permlane32_swap_b32_e32 v99, v101
	v_permlane32_swap_b32_e32 v102, v104
	v_permlane32_swap_b32_e32 v103, v105
	s_mul_i32 s0, s34, 0x110
	v_add_u32_e32 v63, 0xb000, v107
	v_add_u32_e32 v63, s0, v63
	ds_read_b128 v[82:85], v63
	s_branch .LBB0_118
.Lnl_tp0:
	s_cmp_eq_u32 s39, 0
	s_cbranch_scc1 .Lnl_t_done
	v_lshl_or_b32 v63, v86, 8, v107
	v_mov_b64_e32 v[14:15], 0
	v_mov_b64_e32 v[16:17], 0
	s_mov_b64 s[0:1], exec
	s_bfm_b64 exec, s39, 0
	global_load_dwordx4 v[14:17], v63, s[28:29] sc0 nt
	s_mov_b64 exec, s[0:1]
	s_branch .Lnl_t_done
.Lnl_tp1:
	s_cmp_eq_u32 s39, 0
	s_cbranch_scc1 .Lnl_t_done
	v_lshl_or_b32 v63, v87, 8, v107
	v_mov_b64_e32 v[18:19], 0
	v_mov_b64_e32 v[20:21], 0
	s_mov_b64 s[0:1], exec
	s_bfm_b64 exec, s39, 0
	global_load_dwordx4 v[18:21], v63, s[28:29] sc0 nt
	s_mov_b64 exec, s[0:1]
	s_branch .Lnl_t_done
.Lnl_tp2:
	s_cmp_eq_u32 s39, 0
	s_cbranch_scc1 .Lnl_t_done
	v_lshl_or_b32 v63, v88, 8, v107
	v_mov_b64_e32 v[22:23], 0
	v_mov_b64_e32 v[24:25], 0
	s_mov_b64 s[0:1], exec
	s_bfm_b64 exec, s39, 0
	global_load_dwordx4 v[22:25], v63, s[28:29] sc0 nt
	s_mov_b64 exec, s[0:1]
	s_branch .Lnl_t_done
.Lnl_tp3:
	s_cmp_eq_u32 s39, 0
	s_cbranch_scc1 .Lnl_t_done
	v_lshl_or_b32 v63, v89, 8, v107
	v_mov_b64_e32 v[26:27], 0
	v_mov_b64_e32 v[28:29], 0
	s_mov_b64 s[0:1], exec
	s_bfm_b64 exec, s39, 0
	global_load_dwordx4 v[26:29], v63, s[28:29] sc0 nt
	s_mov_b64 exec, s[0:1]
	s_branch .Lnl_t_done
.Lnl_tp4:
	s_cmp_eq_u32 s39, 0
	s_cbranch_scc1 .Lnl_t_done
	v_lshl_or_b32 v63, v90, 8, v107
	v_mov_b64_e32 v[30:31], 0
	v_mov_b64_e32 v[32:33], 0
	s_mov_b64 s[0:1], exec
	s_bfm_b64 exec, s39, 0
	global_load_dwordx4 v[30:33], v63, s[28:29] sc0 nt
	s_mov_b64 exec, s[0:1]
	s_branch .Lnl_t_done
.Lnl_tp5:
	s_cmp_eq_u32 s39, 0
	s_cbranch_scc1 .Lnl_t_done
	v_lshl_or_b32 v63, v91, 8, v107
	v_mov_b64_e32 v[34:35], 0
	v_mov_b64_e32 v[36:37], 0
	s_mov_b64 s[0:1], exec
	s_bfm_b64 exec, s39, 0
	global_load_dwordx4 v[34:37], v63, s[28:29] sc0 nt
	s_mov_b64 exec, s[0:1]
	s_branch .Lnl_t_done
.Lnl_tp6:
	s_cmp_eq_u32 s39, 0
	s_cbranch_scc1 .Lnl_t_done
	v_lshl_or_b32 v63, v92, 8, v107
	v_mov_b64_e32 v[38:39], 0
	v_mov_b64_e32 v[40:41], 0
	s_mov_b64 s[0:1], exec
	s_bfm_b64 exec, s39, 0
	global_load_dwordx4 v[38:41], v63, s[28:29] sc0 nt
	s_mov_b64 exec, s[0:1]
	s_branch .Lnl_t_done
.Lnl_tp7:
	s_cmp_eq_u32 s39, 0
	s_cbranch_scc1 .Lnl_t_done
	v_lshl_or_b32 v63, v93, 8, v107
	v_mov_b64_e32 v[42:43], 0
	v_mov_b64_e32 v[44:45], 0
	s_mov_b64 s[0:1], exec
	s_bfm_b64 exec, s39, 0
	global_load_dwordx4 v[42:45], v63, s[28:29] sc0 nt
	s_mov_b64 exec, s[0:1]
	s_branch .Lnl_t_done
.Lnl_tp8:
	s_cmp_eq_u32 s39, 0
	s_cbranch_scc1 .Lnl_t_done
	v_lshl_or_b32 v63, v94, 8, v107
	v_mov_b64_e32 v[46:47], 0
	v_mov_b64_e32 v[48:49], 0
	s_mov_b64 s[0:1], exec
	s_bfm_b64 exec, s39, 0
	global_load_dwordx4 v[46:49], v63, s[28:29] sc0 nt
	s_mov_b64 exec, s[0:1]
	s_branch .Lnl_t_done
.Lnl_tp9:
	s_cmp_eq_u32 s39, 0
	s_cbranch_scc1 .Lnl_t_done
	v_lshl_or_b32 v63, v95, 8, v107
	v_mov_b64_e32 v[50:51], 0
	v_mov_b64_e32 v[52:53], 0
	s_mov_b64 s[0:1], exec
	s_bfm_b64 exec, s39, 0
	global_load_dwordx4 v[50:53], v63, s[28:29] sc0 nt
	s_mov_b64 exec, s[0:1]
	s_branch .Lnl_t_done
.Lnl_tp10:
	s_cmp_eq_u32 s39, 0
	s_cbranch_scc1 .Lnl_t_done
	v_lshl_or_b32 v63, v96, 8, v107
	v_mov_b64_e32 v[54:55], 0
	v_mov_b64_e32 v[56:57], 0
	s_mov_b64 s[0:1], exec
	s_bfm_b64 exec, s39, 0
	global_load_dwordx4 v[54:57], v63, s[28:29] sc0 nt
	s_mov_b64 exec, s[0:1]
	s_branch .Lnl_t_done
.Lnl_tp11:
	s_cmp_eq_u32 s39, 0
	s_cbranch_scc1 .Lnl_t_done
	v_lshl_or_b32 v63, v97, 8, v107
	v_mov_b64_e32 v[58:59], 0
	v_mov_b64_e32 v[60:61], 0
	s_mov_b64 s[0:1], exec
	s_bfm_b64 exec, s39, 0
	global_load_dwordx4 v[58:61], v63, s[28:29] sc0 nt
	s_mov_b64 exec, s[0:1]
	s_branch .Lnl_t_done
.Lnl_tp12:
	s_cmp_eq_u32 s39, 0
	s_cbranch_scc1 .Lnl_t_done
	v_lshl_or_b32 v63, v98, 8, v107
	v_mov_b64_e32 v[66:67], 0
	v_mov_b64_e32 v[68:69], 0
	s_mov_b64 s[0:1], exec
	s_bfm_b64 exec, s39, 0
	global_load_dwordx4 v[66:69], v63, s[28:29] sc0 nt
	s_mov_b64 exec, s[0:1]
	s_branch .Lnl_t_done
.Lnl_tp13:
	s_cmp_eq_u32 s39, 0
	s_cbranch_scc1 .Lnl_t_done
	v_lshl_or_b32 v63, v99, 8, v107
	v_mov_b64_e32 v[70:71], 0
	v_mov_b64_e32 v[72:73], 0
	s_mov_b64 s[0:1], exec
	s_bfm_b64 exec, s39, 0
	global_load_dwordx4 v[70:73], v63, s[28:29] sc0 nt
	s_mov_b64 exec, s[0:1]
	s_branch .Lnl_t_done
.Lnl_tp14:
	s_cmp_eq_u32 s39, 0
	s_cbranch_scc1 .Lnl_t_done
	v_lshl_or_b32 v63, v100, 8, v107
	v_mov_b64_e32 v[74:75], 0
	v_mov_b64_e32 v[76:77], 0
	s_mov_b64 s[0:1], exec
	s_bfm_b64 exec, s39, 0
	global_load_dwordx4 v[74:77], v63, s[28:29] sc0 nt
	s_mov_b64 exec, s[0:1]
	s_branch .Lnl_t_done
.Lnl_tp15:
	s_cmp_eq_u32 s39, 0
	s_cbranch_scc1 .Lnl_t_done
	v_lshl_or_b32 v63, v101, 8, v107
	v_mov_b64_e32 v[78:79], 0
	v_mov_b64_e32 v[80:81], 0
	s_mov_b64 s[0:1], exec
	s_bfm_b64 exec, s39, 0
	global_load_dwordx4 v[78:81], v63, s[28:29] sc0 nt
	s_mov_b64 exec, s[0:1]
	s_branch .Lnl_t_done
